# final LN kernel: the f32 output stores (never re-read on the GPU) use sc1 nt so they do not allocate in the Infinity Cache
# speedup vs baseline: 1.0008x; 1.0008x over previous
.Lln10_nob1:
	s_cmp_eq_u32 s24, 0
	s_cbranch_scc1 .Lln10_noys
	s_nop 0
	global_store_dwordx4 v2, v[44:47], s[12:13] sc1 nt
	global_store_dwordx4 v3, v[48:51], s[12:13] sc1 nt
